# speedup vs baseline: 1.0096x; 1.0096x over previous
.LBB1_3:
	s_or_b64 exec, exec, s[6:7]
	v_max_f32_e32 v1, v3, v3
	v_max_f32_e32 v1, 0, v1
	s_mov_b32 s0, 0xf800000
	v_mul_f32_e32 v2, 0x4f800000, v1
	v_cmp_gt_f32_e32 vcc, s0, v1
	s_nop 1
	v_cndmask_b32_e32 v1, v1, v2, vcc
	v_sqrt_f32_e32 v2, v1
	s_nop 0
	v_add_u32_e32 v3, -1, v2
	v_fma_f32 v4, -v3, v2, v1
	v_cmp_ge_f32_e64 s[0:1], 0, v4
	v_add_u32_e32 v4, 1, v2
	s_nop 0
	v_cndmask_b32_e64 v3, v2, v3, s[0:1]
	v_fma_f32 v2, -v4, v2, v1
	v_cmp_lt_f32_e64 s[0:1], 0, v2
	s_nop 1
	v_cndmask_b32_e64 v2, v3, v4, s[0:1]
	v_mul_f32_e32 v3, 0x37800000, v2
	v_cndmask_b32_e32 v2, v2, v3, vcc
	v_mov_b32_e32 v3, 0x260
	v_cmp_class_f32_e32 vcc, v1, v3
	s_mov_b32 s0, 0x800000
	s_nop 0
	v_cndmask_b32_e32 v1, v2, v1, vcc
	v_fmaak_f32 v1, 0.5, v1, 0x322bcc77
	v_cmp_gt_f32_e32 vcc, s0, v1
	s_mov_b32 s0, 0x3f317217
	s_nop 0
	v_cndmask_b32_e64 v2, 0, 32, vcc
	v_ldexp_f32 v1, v1, v2
	v_log_f32_e32 v1, v1
	s_nop 0
	v_mul_f32_e32 v2, 0x3f317217, v1
	v_fma_f32 v2, v1, s0, -v2
	v_fmamk_f32 v2, v1, 0x3377d1cf, v2
	s_mov_b32 s0, 0x7f800000
	v_fmac_f32_e32 v2, 0x3f317217, v1
	v_cmp_lt_f32_e64 s[0:1], |v1|, s0
	s_nop 1
	v_cndmask_b32_e64 v1, v1, v2, s[0:1]
	v_mov_b32_e32 v2, 0x41b17218
	v_cndmask_b32_e32 v2, 0, v2, vcc
	v_sub_f32_e32 v1, v1, v2
	s_nop 1
	v_add_f32_dpp v1, v1, v1 quad_perm:[1,0,3,2] row_mask:0xf bank_mask:0xf
	s_nop 1
	v_add_f32_dpp v1, v1, v1 quad_perm:[2,3,0,1] row_mask:0xf bank_mask:0xf
	s_nop 1
	v_add_f32_dpp v1, v1, v1 row_half_mirror row_mask:0xf bank_mask:0xf
	s_nop 1
	v_add_f32_dpp v1, v1, v1 row_mirror row_mask:0xf bank_mask:0xf
	v_mov_b32_e32 v2, v1
	s_nop 1
	v_permlane32_swap_b32_e32 v1, v2
	v_add_f32_e32 v1, v1, v2
	v_mov_b32_e32 v2, v1
	s_nop 1
	v_permlane16_swap_b32_e32 v1, v2
	v_add_f32_e32 v1, v1, v2
	v_mov_b32_e32 v2, 0
	v_and_b32_e32 v3, 63, v0
	v_cmp_eq_u32_e32 vcc, 0, v3
	s_and_saveexec_b64 s[0:1], vcc
	s_cbranch_execz .LBB1_5
	v_lshrrev_b32_e32 v3, 4, v0
	s_waitcnt lgkmcnt(0)
	v_add_f32_e32 v1, v1, v2
	ds_write_b32 v3, v1
